# code placement: one s_nop ahead of each MFMA loop whose head sat at 4 mod 8 bytes, so all eleven loop heads start on an 8-byte phase
# baseline (speedup 1.0000x reference)
.LBB0_241:
	v_mov_b32_e32 v0, 0
	v_readlane_b32 s36, v252, 24
	s_add_i32 s0, s8, 0x40080
	s_add_i32 s1, s9, 0x100
	s_mov_b32 s2, -2
	v_mov_b32_e32 v1, v0
	v_mov_b32_e32 v2, v0
	v_mov_b32_e32 v3, v0
	v_mov_b32_e32 v4, v0
	v_mov_b32_e32 v5, v0
	v_mov_b32_e32 v6, v0
	v_mov_b32_e32 v7, v0
	v_mov_b32_e32 v8, v0
	v_mov_b32_e32 v9, v0
	v_mov_b32_e32 v10, v0
	v_mov_b32_e32 v11, v0
	s_waitcnt vmcnt(28)
	v_mov_b32_e32 v12, v0
	v_mov_b32_e32 v13, v0
	v_mov_b32_e32 v14, v0
	v_mov_b32_e32 v15, v0
	s_waitcnt vmcnt(27)
	v_mov_b32_e32 v16, v0
	v_mov_b32_e32 v17, v0
	v_mov_b32_e32 v18, v0
	v_mov_b32_e32 v19, v0
	s_waitcnt vmcnt(26)
	v_mov_b32_e32 v20, v0
	v_mov_b32_e32 v21, v0
	v_mov_b32_e32 v22, v0
	v_mov_b32_e32 v23, v0
	s_waitcnt vmcnt(25)
	v_mov_b32_e32 v24, v0
	v_mov_b32_e32 v25, v0
	v_mov_b32_e32 v26, v0
	v_mov_b32_e32 v27, v0
	s_waitcnt vmcnt(24)
	v_mov_b32_e32 v28, v0
	v_mov_b32_e32 v29, v0
	v_mov_b32_e32 v30, v0
	v_mov_b32_e32 v31, v0
	s_waitcnt vmcnt(23)
	v_mov_b32_e32 v32, v0
	v_mov_b32_e32 v33, v0
	v_mov_b32_e32 v34, v0
	v_mov_b32_e32 v35, v0
	s_waitcnt vmcnt(22)
	v_mov_b32_e32 v36, v0
	v_mov_b32_e32 v37, v0
	v_mov_b32_e32 v38, v0
	v_mov_b32_e32 v39, v0
	s_waitcnt vmcnt(21)
	v_mov_b32_e32 v40, v0
	v_mov_b32_e32 v41, v0
	v_mov_b32_e32 v42, v0
	v_mov_b32_e32 v43, v0
	s_waitcnt vmcnt(20)
	v_mov_b32_e32 v44, v0
	v_mov_b32_e32 v45, v0
	v_mov_b32_e32 v46, v0
	v_mov_b32_e32 v47, v0
	s_waitcnt vmcnt(19)
	v_mov_b32_e32 v48, v0
	v_mov_b32_e32 v49, v0
	v_mov_b32_e32 v50, v0
	v_mov_b32_e32 v51, v0
	s_waitcnt vmcnt(18)
	v_mov_b32_e32 v52, v0
	v_mov_b32_e32 v53, v0
	v_mov_b32_e32 v54, v0
	v_mov_b32_e32 v55, v0
	s_waitcnt vmcnt(17)
	v_mov_b32_e32 v56, v0
	v_mov_b32_e32 v57, v0
	v_mov_b32_e32 v58, v0
	v_mov_b32_e32 v59, v0
	s_waitcnt vmcnt(16)
	v_mov_b32_e32 v60, v0
	v_mov_b32_e32 v61, v0
	v_mov_b32_e32 v62, v0
	v_mov_b32_e32 v63, v0
	v_mov_b32_e32 v64, v0
	v_mov_b32_e32 v65, v0
	v_mov_b32_e32 v66, v0
	v_mov_b32_e32 v67, v0
	s_waitcnt vmcnt(15)
	v_mov_b32_e32 v68, v0
	v_mov_b32_e32 v69, v0
	s_waitcnt vmcnt(14)
	v_mov_b32_e32 v70, v0
	v_mov_b32_e32 v71, v0
	v_mov_b32_e32 v72, v0
	v_mov_b32_e32 v73, v0
	v_mov_b32_e32 v74, v0
	v_mov_b32_e32 v75, v0
	v_mov_b32_e32 v76, v0
	v_mov_b32_e32 v77, v0
	v_mov_b32_e32 v78, v0
	v_mov_b32_e32 v79, v0
	v_mov_b32_e32 v80, v0
	v_mov_b32_e32 v81, v0
	v_mov_b32_e32 v82, v0
	v_mov_b32_e32 v83, v0
	v_mov_b32_e32 v84, v0
	v_mov_b32_e32 v85, v0
	v_mov_b32_e32 v86, v0
	v_mov_b32_e32 v87, v0
	v_mov_b32_e32 v88, v0
	v_mov_b32_e32 v89, v0
	v_mov_b32_e32 v90, v0
	v_mov_b32_e32 v91, v0
	v_mov_b32_e32 v92, v0
	v_mov_b32_e32 v93, v0
	v_mov_b32_e32 v94, v0
	v_mov_b32_e32 v95, v0
	v_mov_b32_e32 v96, v0
	v_mov_b32_e32 v97, v0
	v_mov_b32_e32 v98, v0
	v_mov_b32_e32 v99, v0
	v_mov_b32_e32 v100, v0
	v_mov_b32_e32 v101, v0
	v_mov_b32_e32 v102, v0
	v_mov_b32_e32 v103, v0
	v_mov_b32_e32 v104, v0
	v_mov_b32_e32 v105, v0
	v_mov_b32_e32 v106, v0
	v_mov_b32_e32 v107, v0
	v_mov_b32_e32 v108, v0
	v_mov_b32_e32 v109, v0
	v_mov_b32_e32 v110, v0
	v_mov_b32_e32 v111, v0
	v_mov_b32_e32 v112, v0
	v_mov_b32_e32 v113, v0
	v_mov_b32_e32 v114, v0
	v_mov_b32_e32 v115, v0
	v_mov_b32_e32 v116, v0
	v_mov_b32_e32 v117, v0
	v_mov_b32_e32 v118, v0
	v_mov_b32_e32 v119, v0
	v_mov_b32_e32 v120, v0
	v_mov_b32_e32 v121, v0
	v_mov_b32_e32 v122, v0
	v_mov_b32_e32 v123, v0
	v_mov_b32_e32 v124, v0
	v_mov_b32_e32 v125, v0
	v_mov_b32_e32 v126, v0
	v_mov_b32_e32 v127, v0
	v_readlane_b32 s50, v252, 38
	v_readlane_b32 s37, v252, 25
	v_readlane_b32 s38, v252, 26
	v_readlane_b32 s39, v252, 27
	v_readlane_b32 s40, v252, 28
	v_readlane_b32 s41, v252, 29
	v_readlane_b32 s42, v252, 30
	v_readlane_b32 s43, v252, 31
	v_readlane_b32 s44, v252, 32
	v_readlane_b32 s45, v252, 33
	v_readlane_b32 s46, v252, 34
	v_readlane_b32 s47, v252, 35
	v_readlane_b32 s48, v252, 36
	v_readlane_b32 s49, v252, 37
	v_readlane_b32 s51, v252, 39
	s_nop 0

.LBB0_595:
	s_xor_b64 s[18:19], s[0:1], -1
	s_and_b64 s[0:1], s[0:1], exec
	s_cselect_b32 s0, s96, s93
	s_lshl_b32 s1, s0, 18
	s_mov_b32 m0, s11
	s_or_b32 s13, s1, s95
	buffer_load_dwordx4 v163, s[4:7], s13 offen lds
	s_mov_b32 m0, s29
	s_mov_b32 s42, s6
	buffer_load_dwordx4 v165, s[4:7], s13 offen lds
	s_mov_b32 s43, s7
	s_mov_b32 m0, s22
	s_or_b32 s14, s13, 0x80
	buffer_load_dwordx4 v163, s[40:43], s95 offen lds
	s_mov_b32 m0, s30
	s_lshl_b32 s20, s0, 2
	buffer_load_dwordx4 v165, s[40:43], s95 offen lds
	s_mov_b32 m0, s23
	s_lshl_b32 s25, s0, 17
	buffer_load_dwordx4 v163, s[4:7], s14 offen lds
	s_mov_b32 m0, s31
	s_lshl_b32 s12, s0, 7
	buffer_load_dwordx4 v165, s[4:7], s14 offen lds
	s_mov_b32 m0, s26
	v_mov_b32_e32 v32, 0
	buffer_load_dwordx4 v163, s[40:43], s97 offen lds
	s_mov_b32 m0, s44
	s_mov_b32 s15, 2
	buffer_load_dwordx4 v165, s[40:43], s97 offen lds
	s_waitcnt vmcnt(4)
	s_or_b32 s21, s20, 2
	s_add_i32 s33, s25, 0x20000
	s_mov_b32 s36, 0
	s_mov_b32 s37, 4
	s_mov_b32 s48, 3
	s_mov_b32 s49, 5
	s_mov_b32 s52, 1
	s_mov_b32 s53, s12
	s_mov_b32 s55, s47
	s_mov_b32 s80, s46
	s_mov_b32 s81, 0
	v_mov_b32_e32 v33, v32
	v_mov_b32_e32 v34, v32
	v_mov_b32_e32 v35, v32
	v_mov_b32_e32 v36, v32
	v_mov_b32_e32 v37, v32
	v_mov_b32_e32 v38, v32
	v_mov_b32_e32 v39, v32
	v_mov_b32_e32 v64, v32
	v_mov_b32_e32 v65, v32
	v_mov_b32_e32 v66, v32
	v_mov_b32_e32 v67, v32
	v_mov_b32_e32 v68, v32
	v_mov_b32_e32 v69, v32
	v_mov_b32_e32 v70, v32
	v_mov_b32_e32 v71, v32
	v_mov_b32_e32 v96, v32
	v_mov_b32_e32 v97, v32
	v_mov_b32_e32 v98, v32
	v_mov_b32_e32 v99, v32
	v_mov_b32_e32 v100, v32
	v_mov_b32_e32 v101, v32
	v_mov_b32_e32 v102, v32
	v_mov_b32_e32 v103, v32
	v_mov_b32_e32 v128, v32
	v_mov_b32_e32 v129, v32
	v_mov_b32_e32 v130, v32
	v_mov_b32_e32 v131, v32
	v_mov_b32_e32 v132, v32
	v_mov_b32_e32 v133, v32
	v_mov_b32_e32 v134, v32
	v_mov_b32_e32 v135, v32
	v_mov_b32_e32 v40, v32
	v_mov_b32_e32 v41, v32
	v_mov_b32_e32 v42, v32
	v_mov_b32_e32 v43, v32
	v_mov_b32_e32 v44, v32
	v_mov_b32_e32 v45, v32
	v_mov_b32_e32 v46, v32
	v_mov_b32_e32 v47, v32
	v_mov_b32_e32 v72, v32
	v_mov_b32_e32 v73, v32
	v_mov_b32_e32 v74, v32
	v_mov_b32_e32 v75, v32
	v_mov_b32_e32 v76, v32
	v_mov_b32_e32 v77, v32
	v_mov_b32_e32 v78, v32
	v_mov_b32_e32 v79, v32
	v_mov_b32_e32 v104, v32
	v_mov_b32_e32 v105, v32
	v_mov_b32_e32 v106, v32
	v_mov_b32_e32 v107, v32
	v_mov_b32_e32 v108, v32
	v_mov_b32_e32 v109, v32
	v_mov_b32_e32 v110, v32
	v_mov_b32_e32 v111, v32
	v_mov_b32_e32 v136, v32
	v_mov_b32_e32 v137, v32
	v_mov_b32_e32 v138, v32
	v_mov_b32_e32 v139, v32
	v_mov_b32_e32 v140, v32
	v_mov_b32_e32 v141, v32
	v_mov_b32_e32 v142, v32
	v_mov_b32_e32 v143, v32
	v_mov_b32_e32 v48, v32
	v_mov_b32_e32 v49, v32
	v_mov_b32_e32 v50, v32
	v_mov_b32_e32 v51, v32
	v_mov_b32_e32 v52, v32
	v_mov_b32_e32 v53, v32
	v_mov_b32_e32 v54, v32
	v_mov_b32_e32 v55, v32
	v_mov_b32_e32 v80, v32
	v_mov_b32_e32 v81, v32
	v_mov_b32_e32 v82, v32
	v_mov_b32_e32 v83, v32
	v_mov_b32_e32 v84, v32
	v_mov_b32_e32 v85, v32
	v_mov_b32_e32 v86, v32
	v_mov_b32_e32 v87, v32
	v_mov_b32_e32 v112, v32
	v_mov_b32_e32 v113, v32
	v_mov_b32_e32 v114, v32
	v_mov_b32_e32 v115, v32
	v_mov_b32_e32 v116, v32
	v_mov_b32_e32 v117, v32
	v_mov_b32_e32 v118, v32
	v_mov_b32_e32 v119, v32
	v_mov_b32_e32 v144, v32
	v_mov_b32_e32 v145, v32
	v_mov_b32_e32 v146, v32
	v_mov_b32_e32 v147, v32
	v_mov_b32_e32 v148, v32
	v_mov_b32_e32 v149, v32
	v_mov_b32_e32 v150, v32
	v_mov_b32_e32 v151, v32
	v_mov_b32_e32 v56, v32
	v_mov_b32_e32 v57, v32
	v_mov_b32_e32 v58, v32
	v_mov_b32_e32 v59, v32
	v_mov_b32_e32 v60, v32
	v_mov_b32_e32 v61, v32
	v_mov_b32_e32 v62, v32
	v_mov_b32_e32 v63, v32
	v_mov_b32_e32 v88, v32
	v_mov_b32_e32 v89, v32
	v_mov_b32_e32 v90, v32
	v_mov_b32_e32 v91, v32
	v_mov_b32_e32 v92, v32
	v_mov_b32_e32 v93, v32
	v_mov_b32_e32 v94, v32
	v_mov_b32_e32 v95, v32
	v_mov_b32_e32 v120, v32
	v_mov_b32_e32 v121, v32
	v_mov_b32_e32 v122, v32
	v_mov_b32_e32 v123, v32
	v_mov_b32_e32 v124, v32
	v_mov_b32_e32 v125, v32
	v_mov_b32_e32 v126, v32
	v_mov_b32_e32 v127, v32
	v_mov_b32_e32 v152, v32
	v_mov_b32_e32 v153, v32
	v_mov_b32_e32 v154, v32
	v_mov_b32_e32 v155, v32
	v_mov_b32_e32 v156, v32
	v_mov_b32_e32 v157, v32
	v_mov_b32_e32 v158, v32
	v_mov_b32_e32 v159, v32
	s_barrier
	s_waitcnt vmcnt(0)
	s_branch .LBB0_597
	s_nop 0

.LBB0_781:
	v_mov_b32_e32 v32, 0
	v_readlane_b32 s64, v252, 24
	s_add_i32 s8, s13, 0x80080
	s_add_i32 s9, s12, 0x100
	s_mov_b32 s12, -2
	v_mov_b32_e32 v33, v32
	v_mov_b32_e32 v34, v32
	v_mov_b32_e32 v35, v32
	v_mov_b32_e32 v36, v32
	v_mov_b32_e32 v37, v32
	v_mov_b32_e32 v38, v32
	v_mov_b32_e32 v39, v32
	v_mov_b32_e32 v48, v32
	v_mov_b32_e32 v49, v32
	v_mov_b32_e32 v50, v32
	v_mov_b32_e32 v51, v32
	v_mov_b32_e32 v52, v32
	v_mov_b32_e32 v53, v32
	v_mov_b32_e32 v54, v32
	v_mov_b32_e32 v55, v32
	v_mov_b32_e32 v64, v32
	v_mov_b32_e32 v65, v32
	v_mov_b32_e32 v66, v32
	v_mov_b32_e32 v67, v32
	v_mov_b32_e32 v68, v32
	v_mov_b32_e32 v69, v32
	v_mov_b32_e32 v70, v32
	v_mov_b32_e32 v71, v32
	v_mov_b32_e32 v80, v32
	v_mov_b32_e32 v81, v32
	v_mov_b32_e32 v82, v32
	v_mov_b32_e32 v83, v32
	v_mov_b32_e32 v84, v32
	v_mov_b32_e32 v85, v32
	v_mov_b32_e32 v86, v32
	v_mov_b32_e32 v87, v32
	v_mov_b32_e32 v40, v32
	v_mov_b32_e32 v41, v32
	v_mov_b32_e32 v42, v32
	v_mov_b32_e32 v43, v32
	v_mov_b32_e32 v44, v32
	v_mov_b32_e32 v45, v32
	v_mov_b32_e32 v46, v32
	v_mov_b32_e32 v47, v32
	v_mov_b32_e32 v56, v32
	v_mov_b32_e32 v57, v32
	v_mov_b32_e32 v58, v32
	v_mov_b32_e32 v59, v32
	v_mov_b32_e32 v60, v32
	v_mov_b32_e32 v61, v32
	v_mov_b32_e32 v62, v32
	v_mov_b32_e32 v63, v32
	v_mov_b32_e32 v72, v32
	v_mov_b32_e32 v73, v32
	v_mov_b32_e32 v74, v32
	v_mov_b32_e32 v75, v32
	v_mov_b32_e32 v76, v32
	v_mov_b32_e32 v77, v32
	v_mov_b32_e32 v78, v32
	v_mov_b32_e32 v79, v32
	v_mov_b32_e32 v88, v32
	v_mov_b32_e32 v89, v32
	v_mov_b32_e32 v90, v32
	v_mov_b32_e32 v91, v32
	v_mov_b32_e32 v92, v32
	v_mov_b32_e32 v93, v32
	v_mov_b32_e32 v94, v32
	v_mov_b32_e32 v95, v32
	v_mov_b32_e32 v96, v32
	v_mov_b32_e32 v97, v32
	v_mov_b32_e32 v98, v32
	v_mov_b32_e32 v99, v32
	v_mov_b32_e32 v100, v32
	v_mov_b32_e32 v101, v32
	v_mov_b32_e32 v102, v32
	v_mov_b32_e32 v103, v32
	v_mov_b32_e32 v112, v32
	v_mov_b32_e32 v113, v32
	v_mov_b32_e32 v114, v32
	v_mov_b32_e32 v115, v32
	v_mov_b32_e32 v116, v32
	v_mov_b32_e32 v117, v32
	v_mov_b32_e32 v118, v32
	v_mov_b32_e32 v119, v32
	v_mov_b32_e32 v128, v32
	v_mov_b32_e32 v129, v32
	v_mov_b32_e32 v130, v32
	v_mov_b32_e32 v131, v32
	v_mov_b32_e32 v132, v32
	v_mov_b32_e32 v133, v32
	v_mov_b32_e32 v134, v32
	v_mov_b32_e32 v135, v32
	v_mov_b32_e32 v144, v32
	v_mov_b32_e32 v145, v32
	v_mov_b32_e32 v146, v32
	v_mov_b32_e32 v147, v32
	v_mov_b32_e32 v148, v32
	v_mov_b32_e32 v149, v32
	v_mov_b32_e32 v150, v32
	v_mov_b32_e32 v151, v32
	v_mov_b32_e32 v104, v32
	v_mov_b32_e32 v105, v32
	v_mov_b32_e32 v106, v32
	v_mov_b32_e32 v107, v32
	v_mov_b32_e32 v108, v32
	v_mov_b32_e32 v109, v32
	v_mov_b32_e32 v110, v32
	v_mov_b32_e32 v111, v32
	v_mov_b32_e32 v120, v32
	v_mov_b32_e32 v121, v32
	v_mov_b32_e32 v122, v32
	v_mov_b32_e32 v123, v32
	v_mov_b32_e32 v124, v32
	v_mov_b32_e32 v125, v32
	v_mov_b32_e32 v126, v32
	v_mov_b32_e32 v127, v32
	v_mov_b32_e32 v136, v32
	v_mov_b32_e32 v137, v32
	v_mov_b32_e32 v138, v32
	v_mov_b32_e32 v139, v32
	v_mov_b32_e32 v140, v32
	v_mov_b32_e32 v141, v32
	v_mov_b32_e32 v142, v32
	v_mov_b32_e32 v143, v32
	v_mov_b32_e32 v152, v32
	v_mov_b32_e32 v153, v32
	v_mov_b32_e32 v154, v32
	v_mov_b32_e32 v155, v32
	v_mov_b32_e32 v156, v32
	v_mov_b32_e32 v157, v32
	v_mov_b32_e32 v158, v32
	v_mov_b32_e32 v159, v32
	v_readlane_b32 s78, v252, 38
	v_readlane_b32 s65, v252, 25
	v_readlane_b32 s66, v252, 26
	v_readlane_b32 s67, v252, 27
	v_readlane_b32 s68, v252, 28
	v_readlane_b32 s69, v252, 29
	v_readlane_b32 s70, v252, 30
	v_readlane_b32 s71, v252, 31
	v_readlane_b32 s72, v252, 32
	v_readlane_b32 s73, v252, 33
	v_readlane_b32 s74, v252, 34
	v_readlane_b32 s75, v252, 35
	v_readlane_b32 s76, v252, 36
	v_readlane_b32 s77, v252, 37
	v_readlane_b32 s79, v252, 39
	s_nop 0

.LBB0_964:
	v_mov_b32_e32 v0, 0
	v_readlane_b32 s64, v252, 24
	s_add_i32 s0, s15, 0x40080
	s_add_i32 s1, s14, 0x100
	s_mov_b32 s14, -2
	v_mov_b32_e32 v1, v0
	v_mov_b32_e32 v2, v0
	v_mov_b32_e32 v3, v0
	v_mov_b32_e32 v4, v0
	v_mov_b32_e32 v5, v0
	v_mov_b32_e32 v6, v0
	v_mov_b32_e32 v7, v0
	v_mov_b32_e32 v8, v0
	v_mov_b32_e32 v9, v0
	s_waitcnt vmcnt(24)
	v_mov_b32_e32 v10, v0
	v_mov_b32_e32 v11, v0
	s_waitcnt vmcnt(23)
	v_mov_b32_e32 v12, v0
	v_mov_b32_e32 v13, v0
	s_waitcnt vmcnt(22)
	v_mov_b32_e32 v14, v0
	v_mov_b32_e32 v15, v0
	v_mov_b32_e32 v16, v0
	v_mov_b32_e32 v17, v0
	v_mov_b32_e32 v18, v0
	v_mov_b32_e32 v19, v0
	v_mov_b32_e32 v20, v0
	v_mov_b32_e32 v21, v0
	v_mov_b32_e32 v22, v0
	v_mov_b32_e32 v23, v0
	v_mov_b32_e32 v24, v0
	v_mov_b32_e32 v25, v0
	v_mov_b32_e32 v26, v0
	v_mov_b32_e32 v27, v0
	v_mov_b32_e32 v28, v0
	v_mov_b32_e32 v29, v0
	v_mov_b32_e32 v30, v0
	v_mov_b32_e32 v31, v0
	v_mov_b32_e32 v32, v0
	v_mov_b32_e32 v33, v0
	v_mov_b32_e32 v34, v0
	v_mov_b32_e32 v35, v0
	v_mov_b32_e32 v36, v0
	v_mov_b32_e32 v37, v0
	v_mov_b32_e32 v38, v0
	v_mov_b32_e32 v39, v0
	v_mov_b32_e32 v40, v0
	v_mov_b32_e32 v41, v0
	v_mov_b32_e32 v42, v0
	v_mov_b32_e32 v43, v0
	v_mov_b32_e32 v44, v0
	v_mov_b32_e32 v45, v0
	v_mov_b32_e32 v46, v0
	v_mov_b32_e32 v47, v0
	v_mov_b32_e32 v48, v0
	v_mov_b32_e32 v49, v0
	v_mov_b32_e32 v50, v0
	v_mov_b32_e32 v51, v0
	v_mov_b32_e32 v52, v0
	v_mov_b32_e32 v53, v0
	v_mov_b32_e32 v54, v0
	v_mov_b32_e32 v55, v0
	v_mov_b32_e32 v56, v0
	v_mov_b32_e32 v57, v0
	v_mov_b32_e32 v58, v0
	v_mov_b32_e32 v59, v0
	v_mov_b32_e32 v60, v0
	v_mov_b32_e32 v61, v0
	v_mov_b32_e32 v62, v0
	v_mov_b32_e32 v63, v0
	v_mov_b32_e32 v64, v0
	v_mov_b32_e32 v65, v0
	v_mov_b32_e32 v66, v0
	v_mov_b32_e32 v67, v0
	v_mov_b32_e32 v68, v0
	v_mov_b32_e32 v69, v0
	v_mov_b32_e32 v70, v0
	v_mov_b32_e32 v71, v0
	v_mov_b32_e32 v72, v0
	v_mov_b32_e32 v73, v0
	v_mov_b32_e32 v74, v0
	v_mov_b32_e32 v75, v0
	v_mov_b32_e32 v76, v0
	v_mov_b32_e32 v77, v0
	v_mov_b32_e32 v78, v0
	v_mov_b32_e32 v79, v0
	v_mov_b32_e32 v80, v0
	v_mov_b32_e32 v81, v0
	v_mov_b32_e32 v82, v0
	v_mov_b32_e32 v83, v0
	v_mov_b32_e32 v84, v0
	v_mov_b32_e32 v85, v0
	v_mov_b32_e32 v86, v0
	v_mov_b32_e32 v87, v0
	v_mov_b32_e32 v88, v0
	v_mov_b32_e32 v89, v0
	v_mov_b32_e32 v90, v0
	v_mov_b32_e32 v91, v0
	v_mov_b32_e32 v92, v0
	v_mov_b32_e32 v93, v0
	v_mov_b32_e32 v94, v0
	v_mov_b32_e32 v95, v0
	v_mov_b32_e32 v96, v0
	v_mov_b32_e32 v97, v0
	v_mov_b32_e32 v98, v0
	v_mov_b32_e32 v99, v0
	v_mov_b32_e32 v100, v0
	v_mov_b32_e32 v101, v0
	v_mov_b32_e32 v102, v0
	v_mov_b32_e32 v103, v0
	v_mov_b32_e32 v104, v0
	v_mov_b32_e32 v105, v0
	v_mov_b32_e32 v106, v0
	v_mov_b32_e32 v107, v0
	v_mov_b32_e32 v108, v0
	v_mov_b32_e32 v109, v0
	v_mov_b32_e32 v110, v0
	v_mov_b32_e32 v111, v0
	v_mov_b32_e32 v112, v0
	v_mov_b32_e32 v113, v0
	v_mov_b32_e32 v114, v0
	v_mov_b32_e32 v115, v0
	v_mov_b32_e32 v116, v0
	v_mov_b32_e32 v117, v0
	v_mov_b32_e32 v118, v0
	v_mov_b32_e32 v119, v0
	v_mov_b32_e32 v120, v0
	v_mov_b32_e32 v121, v0
	v_mov_b32_e32 v122, v0
	v_mov_b32_e32 v123, v0
	v_mov_b32_e32 v124, v0
	v_mov_b32_e32 v125, v0
	v_mov_b32_e32 v126, v0
	v_mov_b32_e32 v127, v0
	v_readlane_b32 s78, v252, 38
	v_readlane_b32 s65, v252, 25
	v_readlane_b32 s66, v252, 26
	v_readlane_b32 s67, v252, 27
	v_readlane_b32 s68, v252, 28
	v_readlane_b32 s69, v252, 29
	v_readlane_b32 s70, v252, 30
	v_readlane_b32 s71, v252, 31
	v_readlane_b32 s72, v252, 32
	v_readlane_b32 s73, v252, 33
	v_readlane_b32 s74, v252, 34
	v_readlane_b32 s75, v252, 35
	v_readlane_b32 s76, v252, 36
	v_readlane_b32 s77, v252, 37
	v_readlane_b32 s79, v252, 39
	s_nop 0

.LBB0_1157:
	s_waitcnt vmcnt(22)
	v_mov_b32_e32 v32, 0
	v_readlane_b32 s64, v252, 24
	s_add_i32 s8, s13, 0xb0080
	s_add_i32 s9, s12, 0x100
	s_mov_b32 s12, -2
	v_mov_b32_e32 v33, v32
	v_mov_b32_e32 v34, v32
	v_mov_b32_e32 v35, v32
	s_waitcnt vmcnt(21)
	v_mov_b32_e32 v36, v32
	v_mov_b32_e32 v37, v32
	v_mov_b32_e32 v38, v32
	v_mov_b32_e32 v39, v32
	s_waitcnt vmcnt(18)
	v_mov_b32_e32 v48, v32
	v_mov_b32_e32 v49, v32
	v_mov_b32_e32 v50, v32
	v_mov_b32_e32 v51, v32
	s_waitcnt vmcnt(17)
	v_mov_b32_e32 v52, v32
	v_mov_b32_e32 v53, v32
	v_mov_b32_e32 v54, v32
	v_mov_b32_e32 v55, v32
	v_mov_b32_e32 v64, v32
	v_mov_b32_e32 v65, v32
	v_mov_b32_e32 v66, v32
	v_mov_b32_e32 v67, v32
	v_mov_b32_e32 v68, v32
	v_mov_b32_e32 v69, v32
	v_mov_b32_e32 v70, v32
	v_mov_b32_e32 v71, v32
	v_mov_b32_e32 v80, v32
	v_mov_b32_e32 v81, v32
	v_mov_b32_e32 v82, v32
	v_mov_b32_e32 v83, v32
	v_mov_b32_e32 v84, v32
	v_mov_b32_e32 v85, v32
	v_mov_b32_e32 v86, v32
	v_mov_b32_e32 v87, v32
	v_mov_b32_e32 v40, v32
	v_mov_b32_e32 v41, v32
	v_mov_b32_e32 v42, v32
	v_mov_b32_e32 v43, v32
	v_mov_b32_e32 v44, v32
	v_mov_b32_e32 v45, v32
	v_mov_b32_e32 v46, v32
	v_mov_b32_e32 v47, v32
	s_waitcnt vmcnt(16)
	v_mov_b32_e32 v56, v32
	v_mov_b32_e32 v57, v32
	v_mov_b32_e32 v58, v32
	v_mov_b32_e32 v59, v32
	s_waitcnt vmcnt(15)
	v_mov_b32_e32 v60, v32
	v_mov_b32_e32 v61, v32
	v_mov_b32_e32 v62, v32
	v_mov_b32_e32 v63, v32
	v_mov_b32_e32 v72, v32
	v_mov_b32_e32 v73, v32
	v_mov_b32_e32 v74, v32
	v_mov_b32_e32 v75, v32
	v_mov_b32_e32 v76, v32
	v_mov_b32_e32 v77, v32
	v_mov_b32_e32 v78, v32
	v_mov_b32_e32 v79, v32
	v_mov_b32_e32 v88, v32
	v_mov_b32_e32 v89, v32
	v_mov_b32_e32 v90, v32
	v_mov_b32_e32 v91, v32
	v_mov_b32_e32 v92, v32
	v_mov_b32_e32 v93, v32
	v_mov_b32_e32 v94, v32
	v_mov_b32_e32 v95, v32
	v_mov_b32_e32 v96, v32
	v_mov_b32_e32 v97, v32
	v_mov_b32_e32 v98, v32
	v_mov_b32_e32 v99, v32
	v_mov_b32_e32 v100, v32
	v_mov_b32_e32 v101, v32
	v_mov_b32_e32 v102, v32
	v_mov_b32_e32 v103, v32
	v_mov_b32_e32 v112, v32
	v_mov_b32_e32 v113, v32
	v_mov_b32_e32 v114, v32
	v_mov_b32_e32 v115, v32
	v_mov_b32_e32 v116, v32
	v_mov_b32_e32 v117, v32
	v_mov_b32_e32 v118, v32
	v_mov_b32_e32 v119, v32
	v_mov_b32_e32 v128, v32
	v_mov_b32_e32 v129, v32
	v_mov_b32_e32 v130, v32
	v_mov_b32_e32 v131, v32
	v_mov_b32_e32 v132, v32
	v_mov_b32_e32 v133, v32
	v_mov_b32_e32 v134, v32
	v_mov_b32_e32 v135, v32
	v_mov_b32_e32 v144, v32
	v_mov_b32_e32 v145, v32
	v_mov_b32_e32 v146, v32
	v_mov_b32_e32 v147, v32
	v_mov_b32_e32 v148, v32
	v_mov_b32_e32 v149, v32
	v_mov_b32_e32 v150, v32
	v_mov_b32_e32 v151, v32
	v_mov_b32_e32 v104, v32
	v_mov_b32_e32 v105, v32
	v_mov_b32_e32 v106, v32
	v_mov_b32_e32 v107, v32
	v_mov_b32_e32 v108, v32
	v_mov_b32_e32 v109, v32
	v_mov_b32_e32 v110, v32
	v_mov_b32_e32 v111, v32
	v_mov_b32_e32 v120, v32
	v_mov_b32_e32 v121, v32
	v_mov_b32_e32 v122, v32
	v_mov_b32_e32 v123, v32
	v_mov_b32_e32 v124, v32
	v_mov_b32_e32 v125, v32
	v_mov_b32_e32 v126, v32
	v_mov_b32_e32 v127, v32
	v_mov_b32_e32 v136, v32
	v_mov_b32_e32 v137, v32
	v_mov_b32_e32 v138, v32
	v_mov_b32_e32 v139, v32
	v_mov_b32_e32 v140, v32
	v_mov_b32_e32 v141, v32
	v_mov_b32_e32 v142, v32
	v_mov_b32_e32 v143, v32
	v_mov_b32_e32 v152, v32
	v_mov_b32_e32 v153, v32
	v_mov_b32_e32 v154, v32
	v_mov_b32_e32 v155, v32
	v_mov_b32_e32 v156, v32
	v_mov_b32_e32 v157, v32
	v_mov_b32_e32 v158, v32
	v_mov_b32_e32 v159, v32
	v_readlane_b32 s78, v252, 38
	v_readlane_b32 s65, v252, 25
	v_readlane_b32 s66, v252, 26
	v_readlane_b32 s67, v252, 27
	v_readlane_b32 s68, v252, 28
	v_readlane_b32 s69, v252, 29
	v_readlane_b32 s70, v252, 30
	v_readlane_b32 s71, v252, 31
	v_readlane_b32 s72, v252, 32
	v_readlane_b32 s73, v252, 33
	v_readlane_b32 s74, v252, 34
	v_readlane_b32 s75, v252, 35
	v_readlane_b32 s76, v252, 36
	v_readlane_b32 s77, v252, 37
	v_readlane_b32 s79, v252, 39
	s_nop 0

.LBB0_1442:
	v_mov_b32_e32 v32, 0
	v_readlane_b32 s12, v252, 24
	s_add_i32 s0, s81, 0x40080
	s_add_i32 s1, s82, 0x100
	s_mov_b32 s81, -2
	v_mov_b32_e32 v33, v32
	v_mov_b32_e32 v34, v32
	v_mov_b32_e32 v35, v32
	v_mov_b32_e32 v40, v32
	v_mov_b32_e32 v41, v32
	v_mov_b32_e32 v42, v32
	v_mov_b32_e32 v43, v32
	v_mov_b32_e32 v48, v32
	v_mov_b32_e32 v49, v32
	v_mov_b32_e32 v50, v32
	v_mov_b32_e32 v51, v32
	v_mov_b32_e32 v56, v32
	v_mov_b32_e32 v57, v32
	v_mov_b32_e32 v58, v32
	v_mov_b32_e32 v59, v32
	v_mov_b32_e32 v64, v32
	v_mov_b32_e32 v65, v32
	v_mov_b32_e32 v66, v32
	v_mov_b32_e32 v67, v32
	v_mov_b32_e32 v72, v32
	v_mov_b32_e32 v73, v32
	v_mov_b32_e32 v74, v32
	v_mov_b32_e32 v75, v32
	v_mov_b32_e32 v80, v32
	v_mov_b32_e32 v81, v32
	v_mov_b32_e32 v82, v32
	v_mov_b32_e32 v83, v32
	v_mov_b32_e32 v88, v32
	v_mov_b32_e32 v89, v32
	v_mov_b32_e32 v90, v32
	v_mov_b32_e32 v91, v32
	v_mov_b32_e32 v36, v32
	v_mov_b32_e32 v37, v32
	v_mov_b32_e32 v38, v32
	v_mov_b32_e32 v39, v32
	v_mov_b32_e32 v44, v32
	v_mov_b32_e32 v45, v32
	v_mov_b32_e32 v46, v32
	v_mov_b32_e32 v47, v32
	v_mov_b32_e32 v52, v32
	v_mov_b32_e32 v53, v32
	v_mov_b32_e32 v54, v32
	v_mov_b32_e32 v55, v32
	v_mov_b32_e32 v60, v32
	v_mov_b32_e32 v61, v32
	v_mov_b32_e32 v62, v32
	v_mov_b32_e32 v63, v32
	v_mov_b32_e32 v68, v32
	v_mov_b32_e32 v69, v32
	v_mov_b32_e32 v70, v32
	v_mov_b32_e32 v71, v32
	v_mov_b32_e32 v76, v32
	v_mov_b32_e32 v77, v32
	v_mov_b32_e32 v78, v32
	v_mov_b32_e32 v79, v32
	v_mov_b32_e32 v84, v32
	v_mov_b32_e32 v85, v32
	v_mov_b32_e32 v86, v32
	v_mov_b32_e32 v87, v32
	v_mov_b32_e32 v92, v32
	v_mov_b32_e32 v93, v32
	v_mov_b32_e32 v94, v32
	v_mov_b32_e32 v95, v32
	v_mov_b32_e32 v96, v32
	v_mov_b32_e32 v97, v32
	v_mov_b32_e32 v98, v32
	v_mov_b32_e32 v99, v32
	v_mov_b32_e32 v104, v32
	v_mov_b32_e32 v105, v32
	v_mov_b32_e32 v106, v32
	v_mov_b32_e32 v107, v32
	v_mov_b32_e32 v112, v32
	v_mov_b32_e32 v113, v32
	v_mov_b32_e32 v114, v32
	v_mov_b32_e32 v115, v32
	v_mov_b32_e32 v120, v32
	v_mov_b32_e32 v121, v32
	v_mov_b32_e32 v122, v32
	v_mov_b32_e32 v123, v32
	v_mov_b32_e32 v128, v32
	v_mov_b32_e32 v129, v32
	v_mov_b32_e32 v130, v32
	v_mov_b32_e32 v131, v32
	v_mov_b32_e32 v136, v32
	v_mov_b32_e32 v137, v32
	v_mov_b32_e32 v138, v32
	v_mov_b32_e32 v139, v32
	v_mov_b32_e32 v144, v32
	v_mov_b32_e32 v145, v32
	v_mov_b32_e32 v146, v32
	v_mov_b32_e32 v147, v32
	v_mov_b32_e32 v152, v32
	v_mov_b32_e32 v153, v32
	v_mov_b32_e32 v154, v32
	v_mov_b32_e32 v155, v32
	v_mov_b32_e32 v100, v32
	v_mov_b32_e32 v101, v32
	v_mov_b32_e32 v102, v32
	v_mov_b32_e32 v103, v32
	v_mov_b32_e32 v108, v32
	v_mov_b32_e32 v109, v32
	v_mov_b32_e32 v110, v32
	v_mov_b32_e32 v111, v32
	v_mov_b32_e32 v116, v32
	v_mov_b32_e32 v117, v32
	v_mov_b32_e32 v118, v32
	v_mov_b32_e32 v119, v32
	v_mov_b32_e32 v124, v32
	v_mov_b32_e32 v125, v32
	v_mov_b32_e32 v126, v32
	v_mov_b32_e32 v127, v32
	v_mov_b32_e32 v132, v32
	v_mov_b32_e32 v133, v32
	v_mov_b32_e32 v134, v32
	v_mov_b32_e32 v135, v32
	v_mov_b32_e32 v140, v32
	v_mov_b32_e32 v141, v32
	v_mov_b32_e32 v142, v32
	v_mov_b32_e32 v143, v32
	v_mov_b32_e32 v148, v32
	v_mov_b32_e32 v149, v32
	v_mov_b32_e32 v150, v32
	v_mov_b32_e32 v151, v32
	v_mov_b32_e32 v156, v32
	v_mov_b32_e32 v157, v32
	v_mov_b32_e32 v158, v32
	v_mov_b32_e32 v159, v32
	v_readlane_b32 s26, v252, 38
	v_readlane_b32 s13, v252, 25
	v_readlane_b32 s14, v252, 26
	v_readlane_b32 s15, v252, 27
	v_readlane_b32 s16, v252, 28
	v_readlane_b32 s17, v252, 29
	v_readlane_b32 s18, v252, 30
	v_readlane_b32 s19, v252, 31
	v_readlane_b32 s20, v252, 32
	v_readlane_b32 s21, v252, 33
	v_readlane_b32 s22, v252, 34
	v_readlane_b32 s23, v252, 35
	v_readlane_b32 s24, v252, 36
	v_readlane_b32 s25, v252, 37
	v_readlane_b32 s27, v252, 39
	s_nop 0

.LBB0_1666:
	v_mov_b32_e32 v32, 0
	v_readlane_b32 s64, v252, 24
	s_add_i32 s0, s33, 0x30080
	s_add_i32 s1, s55, 0x100
	s_mov_b32 s33, -2
	v_mov_b32_e32 v33, v32
	v_mov_b32_e32 v34, v32
	v_mov_b32_e32 v35, v32
	v_mov_b32_e32 v36, v32
	v_mov_b32_e32 v37, v32
	v_mov_b32_e32 v38, v32
	v_mov_b32_e32 v39, v32
	v_mov_b32_e32 v48, v32
	v_mov_b32_e32 v49, v32
	v_mov_b32_e32 v50, v32
	v_mov_b32_e32 v51, v32
	v_mov_b32_e32 v52, v32
	v_mov_b32_e32 v53, v32
	v_mov_b32_e32 v54, v32
	v_mov_b32_e32 v55, v32
	v_mov_b32_e32 v64, v32
	v_mov_b32_e32 v65, v32
	v_mov_b32_e32 v66, v32
	v_mov_b32_e32 v67, v32
	v_mov_b32_e32 v68, v32
	v_mov_b32_e32 v69, v32
	v_mov_b32_e32 v70, v32
	v_mov_b32_e32 v71, v32
	v_mov_b32_e32 v80, v32
	v_mov_b32_e32 v81, v32
	v_mov_b32_e32 v82, v32
	v_mov_b32_e32 v83, v32
	v_mov_b32_e32 v84, v32
	v_mov_b32_e32 v85, v32
	v_mov_b32_e32 v86, v32
	v_mov_b32_e32 v87, v32
	v_mov_b32_e32 v40, v32
	v_mov_b32_e32 v41, v32
	v_mov_b32_e32 v42, v32
	v_mov_b32_e32 v43, v32
	v_mov_b32_e32 v44, v32
	v_mov_b32_e32 v45, v32
	v_mov_b32_e32 v46, v32
	v_mov_b32_e32 v47, v32
	v_mov_b32_e32 v56, v32
	v_mov_b32_e32 v57, v32
	v_mov_b32_e32 v58, v32
	v_mov_b32_e32 v59, v32
	v_mov_b32_e32 v60, v32
	v_mov_b32_e32 v61, v32
	v_mov_b32_e32 v62, v32
	v_mov_b32_e32 v63, v32
	v_mov_b32_e32 v72, v32
	v_mov_b32_e32 v73, v32
	v_mov_b32_e32 v74, v32
	v_mov_b32_e32 v75, v32
	v_mov_b32_e32 v76, v32
	v_mov_b32_e32 v77, v32
	v_mov_b32_e32 v78, v32
	v_mov_b32_e32 v79, v32
	v_mov_b32_e32 v88, v32
	v_mov_b32_e32 v89, v32
	v_mov_b32_e32 v90, v32
	v_mov_b32_e32 v91, v32
	v_mov_b32_e32 v92, v32
	v_mov_b32_e32 v93, v32
	v_mov_b32_e32 v94, v32
	v_mov_b32_e32 v95, v32
	v_mov_b32_e32 v96, v32
	v_mov_b32_e32 v97, v32
	v_mov_b32_e32 v98, v32
	v_mov_b32_e32 v99, v32
	v_mov_b32_e32 v100, v32
	v_mov_b32_e32 v101, v32
	v_mov_b32_e32 v102, v32
	v_mov_b32_e32 v103, v32
	v_mov_b32_e32 v112, v32
	v_mov_b32_e32 v113, v32
	v_mov_b32_e32 v114, v32
	v_mov_b32_e32 v115, v32
	v_mov_b32_e32 v116, v32
	v_mov_b32_e32 v117, v32
	v_mov_b32_e32 v118, v32
	v_mov_b32_e32 v119, v32
	v_mov_b32_e32 v128, v32
	v_mov_b32_e32 v129, v32
	v_mov_b32_e32 v130, v32
	v_mov_b32_e32 v131, v32
	v_mov_b32_e32 v132, v32
	v_mov_b32_e32 v133, v32
	v_mov_b32_e32 v134, v32
	v_mov_b32_e32 v135, v32
	v_mov_b32_e32 v144, v32
	v_mov_b32_e32 v145, v32
	v_mov_b32_e32 v146, v32
	v_mov_b32_e32 v147, v32
	v_mov_b32_e32 v148, v32
	v_mov_b32_e32 v149, v32
	v_mov_b32_e32 v150, v32
	v_mov_b32_e32 v151, v32
	v_mov_b32_e32 v104, v32
	v_mov_b32_e32 v105, v32
	v_mov_b32_e32 v106, v32
	v_mov_b32_e32 v107, v32
	v_mov_b32_e32 v108, v32
	v_mov_b32_e32 v109, v32
	v_mov_b32_e32 v110, v32
	v_mov_b32_e32 v111, v32
	v_mov_b32_e32 v120, v32
	v_mov_b32_e32 v121, v32
	v_mov_b32_e32 v122, v32
	v_mov_b32_e32 v123, v32
	v_mov_b32_e32 v124, v32
	v_mov_b32_e32 v125, v32
	v_mov_b32_e32 v126, v32
	v_mov_b32_e32 v127, v32
	v_mov_b32_e32 v136, v32
	v_mov_b32_e32 v137, v32
	v_mov_b32_e32 v138, v32
	v_mov_b32_e32 v139, v32
	v_mov_b32_e32 v140, v32
	v_mov_b32_e32 v141, v32
	v_mov_b32_e32 v142, v32
	v_mov_b32_e32 v143, v32
	v_mov_b32_e32 v152, v32
	v_mov_b32_e32 v153, v32
	v_mov_b32_e32 v154, v32
	v_mov_b32_e32 v155, v32
	v_mov_b32_e32 v156, v32
	v_mov_b32_e32 v157, v32
	v_mov_b32_e32 v158, v32
	v_mov_b32_e32 v159, v32
	v_readlane_b32 s78, v252, 38
	v_readlane_b32 s65, v252, 25
	v_readlane_b32 s66, v252, 26
	v_readlane_b32 s67, v252, 27
	v_readlane_b32 s68, v252, 28
	v_readlane_b32 s69, v252, 29
	v_readlane_b32 s70, v252, 30
	v_readlane_b32 s71, v252, 31
	v_readlane_b32 s72, v252, 32
	v_readlane_b32 s73, v252, 33
	v_readlane_b32 s74, v252, 34
	v_readlane_b32 s75, v252, 35
	v_readlane_b32 s76, v252, 36
	v_readlane_b32 s77, v252, 37
	v_readlane_b32 s79, v252, 39
	s_nop 0
